# P2: half of the workgroups run attention first and the spatial gating unit last
# baseline (speedup 1.0000x reference)
.LBB0_327:
	s_cmp_lt_i32 s84, 3
	s_cselect_b64 s[0:1], -1, 0
	s_cmp_gt_i32 s85, 2
	s_cselect_b64 s[4:5], -1, 0
	s_and_b64 s[0:1], s[0:1], s[4:5]
	s_andn2_b64 vcc, exec, s[0:1]
	s_cbranch_vccnz .LBB0_454
	v_writelane_b32 v254, s88, 48
	s_mov_b32 s0, s96
	s_cmpk_gt_i32 s96, 0xff
	v_writelane_b32 v254, s89, 49
	v_writelane_b32 v254, s90, 50
	s_nop 1
	v_writelane_b32 v254, s91, 51
	v_writelane_b32 v254, s84, 52
	s_nop 1
	v_writelane_b32 v254, s85, 53
	v_writelane_b32 v254, s82, 54
	s_nop 1
	v_writelane_b32 v254, s83, 55
	v_writelane_b32 v254, s76, 56
	s_nop 1
	v_writelane_b32 v254, s77, 57
	s_mov_b32 s76, s86
	v_writelane_b32 v254, s76, 58
	s_nop 1
	v_writelane_b32 v254, s77, 59
	v_writelane_b32 v254, s0, 60
	s_nop 1
	v_writelane_b32 v254, s1, 61
	s_mov_b32 s99, 0
	s_cbranch_scc1 .LBB0_341
	s_bitcmp1_b32 s96, 3
	s_cbranch_scc0 .Lp2_sgu_first
	s_mov_b32 s99, 1
	s_branch .LBB0_341
.Lp2_done_late:
	v_readlane_b32 s88, v254, 48
	v_readlane_b32 s89, v254, 49
	v_readlane_b32 s90, v254, 50
	v_readlane_b32 s91, v254, 51
	v_readlane_b32 s96, v254, 60
	v_readlane_b32 s97, v254, 61
	s_branch .LBB0_400
.Lp2_sgu_late:
	s_mov_b32 s99, 2
.Lp2_sgu_first:
	v_mbcnt_lo_u32_b32 v5, -1, 0
	v_mbcnt_hi_u32_b32 v5, -1, v5
	s_waitcnt vmcnt(0)
	v_and_b32_e32 v7, 64, v5
	v_xor_b32_e32 v6, 1, v5
	v_add_u32_e32 v7, 64, v7
	v_or_b32_e32 v4, 0x200, v0
	v_cmp_lt_i32_e32 vcc, v6, v7
	v_lshrrev_b32_e32 v78, 4, v4
	v_or_b32_e32 v4, 0x600, v0
	v_cndmask_b32_e32 v6, v5, v6, vcc
	v_lshrrev_b32_e32 v75, 4, v4
	v_and_b32_e32 v4, 3, v0
	v_lshlrev_b32_e32 v83, 2, v6
	v_xor_b32_e32 v6, 2, v5
	v_readlane_b32 s4, v254, 13
	v_cmp_lt_i32_e32 vcc, v6, v7
	v_cmp_eq_u32_e64 s[0:1], 0, v4
	v_readlane_b32 s5, v254, 14
	v_readlane_b32 s6, v254, 15
	v_readlane_b32 s7, v254, 16
	v_readlane_b32 s8, v254, 17
	v_readlane_b32 s9, v254, 18
	v_readlane_b32 s10, v254, 19
	v_readlane_b32 s11, v254, 20
	v_readlane_b32 s12, v254, 21
	v_readlane_b32 s13, v254, 22
	v_readlane_b32 s14, v254, 23
	v_readlane_b32 s15, v254, 24
	v_readlane_b32 s16, v254, 25
	v_readlane_b32 s17, v254, 26
	v_readlane_b32 s18, v254, 27
	v_readlane_b32 s19, v254, 28
	v_cndmask_b32_e32 v5, v5, v6, vcc
	v_writelane_b32 v254, s0, 62
	v_lshlrev_b32_e32 v140, 2, v5
	v_and_b32_e32 v5, 0x1fc, v0
	v_writelane_b32 v254, s1, 63
	s_add_i32 s0, 0, 0x10000
	s_add_i32 s1, 0, 0x10200
	v_add_u32_e32 v141, s0, v5
	v_add_u32_e32 v142, s1, v5
	v_and_b32_e32 v5, 15, v0
	v_lshlrev_b32_e32 v3, 3, v0
	v_lshrrev_b32_e32 v74, 4, v0
	v_lshlrev_b32_e32 v7, 3, v5
	v_and_b32_e32 v2, 0x78, v3
	s_mov_b64 s[72:73], s[16:17]
	v_or_b32_e32 v82, 64, v74
	v_or_b32_e32 v19, 2, v7
	v_mov_b32_e32 v71, 0
	v_lshlrev_b32_e32 v70, 2, v2
	s_mov_b64 s[70:71], s[14:15]
	s_mov_b64 s[68:69], s[12:13]
	s_mov_b64 s[66:67], s[10:11]
	s_mov_b64 s[64:65], s[8:9]
	v_cmp_gt_u32_e64 s[12:13], v19, v74
	v_or_b32_e32 v20, 3, v7
	v_lshlrev_b32_e32 v25, 2, v74
	v_cmp_gt_u32_e64 s[28:29], v19, v78
	v_lshlrev_b32_e32 v28, 2, v78
	v_cmp_gt_u32_e64 s[46:47], v19, v82
	v_cmp_gt_u32_e64 s[62:63], v19, v75
	v_lshlrev_b32_e32 v19, 2, v75
	v_lshl_add_u64 v[72:73], s[70:71], 0, v[70:71]
	v_bfe_u32 v8, v0, 6, 2
	v_lshlrev_b32_e32 v70, 2, v0
	v_lshrrev_b32_e32 v16, 3, v1
	v_cmp_gt_u32_e64 s[14:15], v20, v74
	v_and_b32_e32 v26, 12, v25
	v_cmp_gt_u32_e64 s[30:31], v20, v78
	v_and_b32_e32 v29, 12, v28
	v_cmp_gt_u32_e64 s[48:49], v20, v82
	v_cmp_gt_u32_e64 s[6:7], v20, v75
	v_and_b32_e32 v20, 12, v19
	v_and_b32_e32 v9, 12, v70
	v_bfe_u32 v10, v0, 2, 2
	v_and_b32_e32 v15, 12, v0
	v_and_b32_e32 v16, 2, v16
	v_bitop3_b32 v26, v26, v5, v8 bitop3:0x36
	v_bitop3_b32 v29, v29, v5, v8 bitop3:0x36
	v_bitop3_b32 v8, v20, v5, v8 bitop3:0x36
	v_lshlrev_b32_e32 v20, 6, v0
	v_lshrrev_b32_e32 v6, 4, v1
	v_or_b32_e32 v11, v9, v10
	v_bfe_u32 v14, v0, 1, 1
	v_or_b32_e32 v17, v16, v15
	v_cmp_gt_u32_e64 s[8:9], v7, v74
	v_cmp_lt_u32_e64 s[10:11], v7, v74
	v_or_b32_e32 v21, 4, v7
	v_or_b32_e32 v22, 5, v7
	v_or_b32_e32 v23, 6, v7
	v_or_b32_e32 v24, 7, v7
	v_cmp_gt_u32_e64 s[24:25], v7, v78
	v_cmp_lt_u32_e64 s[26:27], v7, v78
	v_add_u32_e32 v146, s0, v28
	v_add_u32_e32 v147, s1, v28
	v_cmp_gt_u32_e64 s[42:43], v7, v82
	v_cmp_lt_u32_e64 s[44:45], v7, v82
	v_lshlrev_b32_e32 v28, 2, v82
	v_cmp_gt_u32_e64 s[58:59], v7, v75
	v_cmp_lt_u32_e64 s[60:61], v7, v75
	v_lshlrev_b32_e32 v7, 8, v75
	v_and_b32_e32 v20, 0x300, v20
	v_cmp_gt_u32_e64 s[18:19], v22, v74
	v_cmp_gt_u32_e64 s[22:23], v24, v74
	v_add_u32_e32 v144, s0, v25
	v_add_u32_e32 v145, s1, v25
	v_cmp_gt_u32_e64 s[36:37], v22, v78
	v_cmp_gt_u32_e64 s[40:41], v24, v78
	v_cmp_gt_u32_e64 s[52:53], v22, v82
	v_cmp_gt_u32_e64 s[56:57], v24, v82
	v_add_u32_e32 v148, s0, v28
	v_add_u32_e32 v149, s1, v28
	v_cmp_gt_u32_e64 s[94:95], v22, v75
	v_cmp_gt_u32_e64 s[90:91], v24, v75
	v_lshl_or_b32 v7, v8, 4, v7
	v_add_u32_e32 v150, s0, v19
	v_add_u32_e32 v151, s1, v19
	v_bitop3_b32 v8, v9, v6, v10 bitop3:0x36
	v_bitop3_b32 v9, v6, v11, 4 bitop3:0x36
	v_bitop3_b32 v10, v6, v11, 8 bitop3:0x36
	v_bitop3_b32 v11, v6, v11, 12 bitop3:0x36
	v_or_b32_e32 v19, v17, v14
	v_lshl_or_b32 v6, v6, 11, v20
	v_or_b32_e32 v20, 2, v14
	v_or_b32_e32 v22, 4, v14
	v_or_b32_e32 v24, 6, v14
	v_or_b32_e32 v30, 8, v14
	v_or_b32_e32 v32, 10, v14
	v_or_b32_e32 v34, 12, v14
	v_or_b32_e32 v14, 14, v14
	v_readlane_b32 s0, v254, 60
	v_cmp_gt_u32_e64 s[16:17], v21, v74
	v_cmp_gt_u32_e64 s[20:21], v23, v74
	v_cmp_gt_u32_e64 s[34:35], v21, v78
	v_cmp_gt_u32_e64 s[38:39], v23, v78
	v_cmp_gt_u32_e64 s[50:51], v21, v82
	v_cmp_gt_u32_e64 s[54:55], v23, v82
	v_cmp_gt_u32_e64 s[84:85], v21, v75
	v_cmp_gt_u32_e64 s[82:83], v23, v75
	v_bitop3_b32 v21, v16, v20, v15 bitop3:0x36
	v_bitop3_b32 v23, v16, v22, v15 bitop3:0x36
	v_bitop3_b32 v28, v16, v24, v15 bitop3:0x36
	v_bitop3_b32 v31, v16, v30, v15 bitop3:0x36
	v_bitop3_b32 v33, v16, v32, v15 bitop3:0x36
	v_bitop3_b32 v35, v16, v34, v15 bitop3:0x36
	v_bitop3_b32 v15, v16, v14, v15 bitop3:0x36
	v_add_u32_e32 v16, 0, v70
	v_lshl_add_u64 v[88:89], s[66:67], 0, v[70:71]
	v_lshl_add_u64 v[90:91], s[68:69], 0, v[70:71]
	v_lshlrev_b32_e32 v70, 4, v4
	v_mov_b32_e32 v4, 0x39405100
	v_readlane_b32 s1, v254, 61
	v_lshlrev_b32_e32 v76, 9, v74
	v_lshrrev_b32_e32 v13, 1, v0
	v_lshl_or_b32 v94, v5, 4, v4
	s_mov_b32 s74, s0
	s_bitcmp1_b32 s0, 0
	v_readlane_b32 s0, v254, 50
	v_lshlrev_b32_e32 v4, 5, v5
	v_lshlrev_b32_e32 v80, 9, v78
	v_readlane_b32 s4, v254, 58
	v_and_b32_e32 v3, 8, v3
	v_lshlrev_b32_e32 v25, 8, v78
	v_bitop3_b32 v13, v17, v13, 1 bitop3:0x72
	v_bitop3_b32 v20, v17, v20, 1 bitop3:0x36
	v_bitop3_b32 v22, v17, v22, 1 bitop3:0x36
	v_bitop3_b32 v24, v17, v24, 1 bitop3:0x36
	v_bitop3_b32 v30, v17, v30, 1 bitop3:0x36
	v_bitop3_b32 v32, v17, v32, 1 bitop3:0x36
	v_bitop3_b32 v34, v17, v34, 1 bitop3:0x36
	v_bitop3_b32 v14, v17, v14, 1 bitop3:0x36
	v_lshl_add_u64 v[92:93], s[92:93], 0, v[70:71]
	s_cselect_b64 s[2:3], -1, 0
	v_readlane_b32 s1, v254, 51
	s_bitcmp1_b32 s0, 0
	v_or_b32_e32 v70, v76, v4
	v_lshlrev_b32_e32 v86, 9, v75
	v_lshl_or_b32 v143, s4, 4, v5
	v_add_u32_e32 v18, 0, v3
	v_lshlrev_b32_e32 v26, 4, v26
	v_lshl_or_b32 v25, v29, 4, v25
	v_lshlrev_b32_e32 v13, 4, v13
	v_lshlrev_b32_e32 v20, 4, v20
	v_lshlrev_b32_e32 v22, 4, v22
	v_lshlrev_b32_e32 v24, 4, v24
	v_and_b32_e32 v29, 48, v0
	v_lshlrev_b32_e32 v30, 4, v30
	v_lshlrev_b32_e32 v32, 4, v32
	v_lshlrev_b32_e32 v34, 4, v34
	v_lshlrev_b32_e32 v14, 4, v14
	s_cselect_b64 s[0:1], -1, 0
	v_lshl_add_u64 v[96:97], s[70:71], 0, v[70:71]
	v_or_b32_e32 v70, v80, v4
	v_readlane_b32 s5, v254, 59
	v_lshl_add_u32 v12, v143, 8, 0
	v_lshl_or_b32 v27, v74, 8, v26
	v_lshl_or_b32 v26, v82, 8, v26
	v_lshlrev_b32_e32 v8, 4, v8
	v_lshlrev_b32_e32 v9, 4, v9
	v_lshlrev_b32_e32 v10, 4, v10
	v_lshlrev_b32_e32 v11, 4, v11
	v_lshl_add_u32 v19, v19, 4, v18
	v_add3_u32 v13, 0, v13, v6
	v_lshl_add_u32 v21, v21, 4, v18
	v_add3_u32 v20, 0, v20, v6
	v_lshl_add_u32 v23, v23, 4, v18
	v_add3_u32 v22, 0, v22, v6
	v_lshl_add_u32 v28, v28, 4, v18
	v_add3_u32 v24, 0, v24, v6
	v_lshl_add_u32 v31, v31, 4, v18
	v_add3_u32 v30, 0, v30, v6
	v_lshl_add_u32 v33, v33, 4, v18
	v_add3_u32 v32, 0, v32, v6
	v_lshl_add_u32 v35, v35, 4, v18
	v_add3_u32 v34, 0, v34, v6
	v_lshl_add_u32 v15, v15, 4, v18
	v_add3_u32 v14, 0, v14, v6
	v_writelane_b32 v253, s0, 0
	v_lshl_add_u64 v[98:99], s[70:71], 0, v[70:71]
	v_add_u32_e32 v5, 0, v4
	v_or_b32_e32 v70, v86, v4
	v_lshrrev_b32_e32 v4, 1, v29
	v_mov_b32_e32 v77, v71
	v_mov_b32_e32 v81, v71
	v_lshlrev_b32_e32 v84, 9, v82
	v_mov_b32_e32 v85, v71
	v_mov_b32_e32 v87, v71
	v_lshrrev_b32_e32 v79, 2, v0
	s_mov_b32 s81, 0
	v_or_b32_e32 v152, 0xfffffe00, v0
	v_add_u32_e32 v153, 0x11400, v16
	v_mov_b32_e32 v95, v71
	v_writelane_b32 v253, s1, 1
	v_add_u32_e32 v154, 0x10400, v5
	v_lshl_add_u64 v[100:101], s[70:71], 0, v[70:71]
	v_or_b32_e32 v102, 0x39404880, v4
	v_mov_b32_e32 v103, v71
	v_or_b32_e32 v104, 0x5f400040, v29
	v_mov_b32_e32 v105, v71
	s_waitcnt lgkmcnt(0)
	v_or_b32_e32 v106, 0x5f400000, v29
	v_mov_b32_e32 v107, v71
	s_movk_i32 s33, 0x7800
	v_lshlrev_b32_e32 v70, 1, v2
	s_mov_b64 s[86:87], 0x800
	v_mov_b32_e32 v155, 0x260
	v_add_u32_e32 v156, 0, v27
	v_add_u32_e32 v157, 0, v25
	v_add_u32_e32 v158, 0, v26
	v_add_u32_e32 v159, 0, v7
	s_mov_b64 s[0:1], 0x10000
	v_add_u32_e32 v160, v12, v8
	v_add_u32_e32 v161, v12, v9
	v_add_u32_e32 v162, v12, v10
	v_add_u32_e32 v163, v12, v11
	v_add_u32_e32 v164, v19, v6
	v_add_u32_e32 v165, v13, v3
	v_add_u32_e32 v166, v21, v6
	v_add_u32_e32 v167, v20, v3
	v_add_u32_e32 v168, v23, v6
	v_add_u32_e32 v169, v22, v3
	v_add_u32_e32 v170, v28, v6
	v_add_u32_e32 v171, v24, v3
	v_add_u32_e32 v172, v31, v6
	v_add_u32_e32 v173, v30, v3
	v_add_u32_e32 v174, v33, v6
	v_add_u32_e32 v175, v32, v3
	v_add_u32_e32 v176, v35, v6
	v_add_u32_e32 v177, v34, v3
	v_add_u32_e32 v178, v15, v6
	v_add_u32_e32 v179, v14, v3
	s_mov_b64 s[4:5], 0x100
	s_mov_b64 s[96:97], 0x80
	s_mov_b32 s88, s74
	s_mov_b32 s89, s74
	s_branch .LBB0_331

.LBB0_341:
	s_cmp_eq_u32 s99, 2
	s_cbranch_scc1 .Lp2_done_late
	v_readlane_b32 s90, v254, 50
	s_abs_i32 s0, s90
	v_cvt_f32_u32_e32 v2, s0
	s_sub_i32 s4, 0, s0
	s_add_i32 s1, s90, 0xbff
	s_xor_b32 s3, s1, s90
	v_rcp_iflag_f32_e32 v2, v2
	s_abs_i32 s1, s1
	s_ashr_i32 s3, s3, 31
	v_readlane_b32 s96, v254, 60
	v_mul_f32_e32 v2, 0x4f7ffffe, v2
	v_cvt_u32_f32_e32 v2, v2
	v_readlane_b32 s88, v254, 48
	v_readlane_b32 s89, v254, 49
	v_readlane_b32 s91, v254, 51
	v_readfirstlane_b32 s5, v2
	s_mul_i32 s4, s4, s5
	s_mul_hi_u32 s4, s5, s4
	s_add_i32 s5, s5, s4
	s_mul_hi_u32 s4, s1, s5
	s_mul_i32 s5, s4, s0
	s_sub_i32 s1, s1, s5
	s_add_i32 s6, s4, 1
	s_sub_i32 s5, s1, s0
	s_cmp_ge_u32 s1, s0
	s_cselect_b32 s4, s6, s4
	s_cselect_b32 s1, s5, s1
	s_add_i32 s5, s4, 1
	s_cmp_ge_u32 s1, s0
	s_cselect_b32 s0, s5, s4
	s_xor_b32 s0, s0, s3
	s_sub_i32 s0, s0, s3
	s_mul_i32 s3, s0, s96
	s_add_i32 s0, s3, s0
	s_min_i32 s2, s0, 0xc00
	s_cmp_ge_i32 s3, s2
	v_readlane_b32 s97, v254, 61
	s_cbranch_scc1 .LBB0_400
	s_mul_hi_i32 s0, s3, 0x2aaaaaab
	s_lshr_b32 s1, s0, 31
	s_lshr_b32 s0, s0, 9
	s_add_i32 s0, s0, s1
	s_mulk_i32 s0, 0xc00
	s_sub_i32 s5, s3, s0
	s_mul_i32 s0, s5, 0x2aab
	v_mul_u32_u24_e32 v2, 0x26b, v0
	s_lshr_b32 s1, s0, 31
	s_ashr_i32 s11, s0, 17
	v_lshrrev_b32_e32 v2, 17, v2
	s_add_i32 s11, s11, s1
	v_mul_i32_i24_e32 v3, 0xffffff2c, v2
	s_mul_i32 s0, s11, -12
	v_add3_u32 v2, v0, v2, v3
	s_add_i32 s0, s0, s5
	v_sub_u32_e32 v3, 0xa0, v2
	v_subrev_u32_e32 v2, 32, v2
	s_movk_i32 s12, 0x81
	s_ashr_i32 s4, s0, 2
	v_cmp_gt_u32_e64 s[6:7], s12, v2
	s_lshl_b32 s16, s4, 1
	s_nop 0
	v_cndmask_b32_e64 v102, 0, v3, s[6:7]
	v_lshlrev_b32_e32 v2, s16, v102
	v_cmp_lt_i32_e32 vcc, 15, v2
	s_and_saveexec_b64 s[0:1], vcc
	v_readlane_b32 s22, v254, 58
	v_readlane_b32 s23, v254, 59
	s_cbranch_execz .LBB0_344
	v_cvt_f32_u32_e32 v2, v2
	s_mov_b32 s8, 0x800000
	s_mov_b32 s9, 0x7f800000
	s_mov_b32 s10, 0x409b43d5
	v_mul_f32_e32 v2, 0x3d800000, v2
	v_cmp_gt_f32_e32 vcc, s8, v2
	s_mov_b32 s8, 0x3f317217
	s_nop 0
	v_cndmask_b32_e64 v3, 0, 32, vcc
	v_ldexp_f32 v2, v2, v3
	v_log_f32_e32 v2, v2
	v_mov_b32_e32 v3, 0x41b17218
	v_cndmask_b32_e32 v3, 0, v3, vcc
	v_mul_f32_e32 v4, 0x3f317217, v2
	v_fma_f32 v4, v2, s8, -v4
	v_fmamk_f32 v4, v2, 0x3377d1cf, v4
	v_fmac_f32_e32 v4, 0x3f317217, v2
	v_cmp_lt_f32_e64 s[8:9], |v2|, s9
	s_nop 1
	v_cndmask_b32_e64 v2, v2, v4, s[8:9]
	v_sub_f32_e32 v2, v2, v3
	v_div_scale_f32 v3, s[8:9], s10, s10, v2
	v_rcp_f32_e32 v4, v3
	s_nop 0
	v_fma_f32 v5, -v3, v4, 1.0
	v_fmac_f32_e32 v4, v5, v4
	v_div_scale_f32 v5, vcc, v2, s10, v2
	s_waitcnt vmcnt(0)
	v_mul_f32_e32 v6, v5, v4
	v_fma_f32 v7, -v3, v6, v5
	v_fmac_f32_e32 v6, v7, v4
	v_fma_f32 v3, -v3, v6, v5
	v_div_fmas_f32 v3, v3, v4, v6
	v_div_fixup_f32 v2, v3, s10, v2
	v_mul_f32_e32 v2, 0x41800000, v2
	v_cvt_i32_f32_e32 v2, v2
	v_min_i32_e32 v2, 15, v2
	v_add_u32_e32 v2, 16, v2

.LBB0_400:
	s_cmp_eq_u32 s99, 1
	s_cbranch_scc1 .Lp2_sgu_late
	v_readlane_b32 s76, v254, 58
	v_readlane_b32 s84, v254, 52
	v_readlane_b32 s77, v254, 59
	v_readlane_b32 s85, v254, 53
	s_mov_b32 s86, s76
	v_readlane_b32 s76, v254, 56
	v_readlane_b32 s82, v254, 54
	s_cmp_gt_i32 s85, 3
	v_readlane_b32 s4, v254, 32
	v_readlane_b32 s77, v254, 57
	v_readlane_b32 s83, v254, 55
	v_readlane_b32 s5, v254, 33
	v_readlane_b32 s6, v254, 34
	v_readlane_b32 s7, v254, 35
	v_readlane_b32 s8, v254, 36
	v_readlane_b32 s9, v254, 37
	v_readlane_b32 s10, v254, 38
	v_readlane_b32 s11, v254, 39
	v_readlane_b32 s12, v254, 40
	v_readlane_b32 s13, v254, 41
	v_readlane_b32 s14, v254, 42
	v_readlane_b32 s15, v254, 43
	v_readlane_b32 s16, v254, 44
	v_readlane_b32 s17, v254, 45
	v_readlane_b32 s18, v254, 46
	v_readlane_b32 s19, v254, 47
	s_cbranch_scc0 .LBB0_454
	s_waitcnt vmcnt(0)
	s_waitcnt vmcnt(0) lgkmcnt(0)
	s_barrier
	s_and_saveexec_b64 s[0:1], s[76:77]
	s_cbranch_execz .LBB0_453
	s_add_i32 s3, 0, 0x25420
	v_mov_b32_e32 v2, s3
	s_waitcnt vmcnt(0) expcnt(0) lgkmcnt(0)
	ds_read_b32 v4, v2
	s_add_i32 s3, 0, 0x25424
	v_mov_b32_e32 v2, s3
	ds_read_b32 v2, v2
	s_waitcnt lgkmcnt(1)
	v_cmp_ne_u32_e32 vcc, 0, v4
	s_cbranch_vccnz .LBB0_417
	v_readlane_b32 s4, v254, 9
	v_readlane_b32 s5, v254, 10
	s_load_dwordx2 s[8:9], s[4:5], 0x4
	s_add_u32 s4, s92, 0x4200
	s_addc_u32 s5, s93, 0
	s_add_u32 s6, s92, 0x4400
	s_addc_u32 s7, s93, 0
	s_waitcnt lgkmcnt(0)
	s_mul_i32 s3, s8, s90
	s_add_u32 s8, s92, 0x4500
	s_mul_i32 s3, s3, s9
	s_addc_u32 s9, s93, 0
	s_add_u32 s10, s92, 0x4600
	s_addc_u32 s11, s93, 0
	s_add_u32 s12, s92, 0x4700
	s_addc_u32 s13, s93, 0
	s_add_u32 s14, s92, 0x4800
	s_addc_u32 s15, s93, 0
	s_add_u32 s16, s92, 0x4900
	s_addc_u32 s17, s93, 0
	s_add_u32 s18, s92, 0x4a00
	s_addc_u32 s19, s93, 0
	s_add_u32 s20, s92, 0x4b00
	s_addc_u32 s21, s93, 0
	s_add_u32 s22, s92, 0x4c00
	s_addc_u32 s23, s93, 0
	s_add_u32 s24, s92, 0x4d00
	s_addc_u32 s25, s93, 0
	s_add_u32 s26, s92, 0x4e00
	s_addc_u32 s27, s93, 0
	s_add_u32 s28, s92, 0x4f00
	s_addc_u32 s29, s93, 0
	s_add_u32 s30, s92, 0x5000
	s_addc_u32 s31, s93, 0
	s_add_u32 s34, s92, 0x5100
	s_addc_u32 s35, s93, 0
	s_add_u32 s36, s92, 0x5200
	s_addc_u32 s37, s93, 0
	s_add_u32 s38, s92, 0x5300
	s_addc_u32 s39, s93, 0
	s_mov_b32 s46, 1
	v_mov_b32_e32 v18, 0
	s_branch .LBB0_405
